# indexer: score insertion switch rewritten as a 4-level scalar branch tree with 4 v_mov per leaf (was up to 96 register copies per insertion)
# speedup vs baseline: 1.0088x; 1.0020x over previous
; #define IX_INS(cc) case cc: _Pragma("unroll") for (int k = 0; k < 4; ++k) sc[(cc) * 4 + k] = s4[k]; break;
; __device__ __forceinline__ void indexer_phase(const Frame& F, const bf16_t* QI, const bf16_t* KI, const float* WI, unsigned* MASK, const pg8::SideConv& SD) {
;     ...
;                 switch (c * 2 + g) { IX_INS(0) IX_INS(1) IX_INS(2) IX_INS(3) IX_INS(4) IX_INS(5) IX_INS(6) IX_INS(7) IX_INS(8) IX_INS(9) IX_INS(10) IX_INS(11) IX_INS(12) IX_INS(13) IX_INS(14) IX_INS(15)
;                                      IX_INS(16) IX_INS(17) IX_INS(18) IX_INS(19) IX_INS(20) IX_INS(21) IX_INS(22) IX_INS(23) IX_INS(24) IX_INS(25) IX_INS(26) IX_INS(27) IX_INS(28) IX_INS(29) IX_INS(30) IX_INS(31) default: break; }
.LBB0_1472:
	s_cmp_gt_u32 s65, 15
	s_cbranch_scc1 .LBB0_1536
	s_cmp_lt_i32 s65, 8
	s_cbranch_scc1 .Lia_0_8
	s_cmp_lt_i32 s65, 12
	s_cbranch_scc1 .Lia_8_12
	s_cmp_lt_i32 s65, 14
	s_cbranch_scc1 .Lia_12_14
	s_cmp_lt_i32 s65, 15
	s_cbranch_scc1 .Lia_14_15
	v_mov_b32_e32 v100, v238
	v_mov_b32_e32 v101, v239
	v_mov_b32_e32 v96, v0
	v_mov_b32_e32 v97, v1
	s_branch .LBB0_1536
.Lia_14_15:
	v_mov_b32_e32 v98, v238
	v_mov_b32_e32 v99, v239
	v_mov_b32_e32 v92, v0
	v_mov_b32_e32 v93, v1
	s_branch .LBB0_1536
.Lia_12_14:
	s_cmp_lt_i32 s65, 13
	s_cbranch_scc1 .Lia_12_13
	v_mov_b32_e32 v108, v238
	v_mov_b32_e32 v109, v239
	v_mov_b32_e32 v106, v0
	v_mov_b32_e32 v107, v1
	s_branch .LBB0_1536
.Lia_12_13:
	v_mov_b32_e32 v116, v238
	v_mov_b32_e32 v117, v239
	v_mov_b32_e32 v114, v0
	v_mov_b32_e32 v115, v1
	s_branch .LBB0_1536
.Lia_8_12:
	s_cmp_lt_i32 s65, 10
	s_cbranch_scc1 .Lia_8_10
	s_cmp_lt_i32 s65, 11
	s_cbranch_scc1 .Lia_10_11
	v_mov_b32_e32 v124, v238
	v_mov_b32_e32 v125, v239
	v_mov_b32_e32 v122, v0
	v_mov_b32_e32 v123, v1
	s_branch .LBB0_1536
.Lia_10_11:
	v_mov_b32_e32 v132, v238
	v_mov_b32_e32 v133, v239
	v_mov_b32_e32 v130, v0
	v_mov_b32_e32 v131, v1
	s_branch .LBB0_1536
.Lia_8_10:
	s_cmp_lt_i32 s65, 9
	s_cbranch_scc1 .Lia_8_9
	v_mov_b32_e32 v140, v238
	v_mov_b32_e32 v141, v239
	v_mov_b32_e32 v138, v0
	v_mov_b32_e32 v139, v1
	s_branch .LBB0_1536
.Lia_8_9:
	v_mov_b32_e32 v148, v238
	v_mov_b32_e32 v149, v239
	v_mov_b32_e32 v146, v0
	v_mov_b32_e32 v147, v1
	s_branch .LBB0_1536
.Lia_0_8:
	s_cmp_lt_i32 s65, 4
	s_cbranch_scc1 .Lia_0_4
	s_cmp_lt_i32 s65, 6
	s_cbranch_scc1 .Lia_4_6
	s_cmp_lt_i32 s65, 7
	s_cbranch_scc1 .Lia_6_7
	v_mov_b32_e32 v156, v238
	v_mov_b32_e32 v157, v239
	v_mov_b32_e32 v154, v0
	v_mov_b32_e32 v155, v1
	s_branch .LBB0_1536
.Lia_6_7:
	v_mov_b32_e32 v164, v238
	v_mov_b32_e32 v165, v239
	v_mov_b32_e32 v162, v0
	v_mov_b32_e32 v163, v1
	s_branch .LBB0_1536
.Lia_4_6:
	s_cmp_lt_i32 s65, 5
	s_cbranch_scc1 .Lia_4_5
	v_mov_b32_e32 v172, v238
	v_mov_b32_e32 v173, v239
	v_mov_b32_e32 v170, v0
	v_mov_b32_e32 v171, v1
	s_branch .LBB0_1536
.Lia_4_5:
	v_mov_b32_e32 v180, v238
	v_mov_b32_e32 v181, v239
	v_mov_b32_e32 v178, v0
	v_mov_b32_e32 v179, v1
	s_branch .LBB0_1536
.Lia_0_4:
	s_cmp_lt_i32 s65, 2
	s_cbranch_scc1 .Lia_0_2
	s_cmp_lt_i32 s65, 3
	s_cbranch_scc1 .Lia_2_3
	v_mov_b32_e32 v188, v238
	v_mov_b32_e32 v189, v239
	v_mov_b32_e32 v186, v0
	v_mov_b32_e32 v187, v1
	s_branch .LBB0_1536
.Lia_2_3:
	v_mov_b32_e32 v196, v238
	v_mov_b32_e32 v197, v239
	v_mov_b32_e32 v194, v0
	v_mov_b32_e32 v195, v1
	s_branch .LBB0_1536
.Lia_0_2:
	s_cmp_lt_i32 s65, 1
	s_cbranch_scc1 .Lia_0_1
	v_mov_b32_e32 v204, v238
	v_mov_b32_e32 v205, v239
	v_mov_b32_e32 v202, v0
	v_mov_b32_e32 v203, v1
	s_branch .LBB0_1536
.Lia_0_1:
	v_mov_b32_e32 v212, v238
	v_mov_b32_e32 v213, v239
	v_mov_b32_e32 v210, v0
	v_mov_b32_e32 v211, v1

; #define IX_INS(cc) case cc: _Pragma("unroll") for (int k = 0; k < 4; ++k) sc[(cc) * 4 + k] = s4[k]; break;
; __device__ __forceinline__ void indexer_phase(const Frame& F, const bf16_t* QI, const bf16_t* KI, const float* WI, unsigned* MASK, const pg8::SideConv& SD) {
;     ...
;                 switch (c * 2 + g) { IX_INS(0) IX_INS(1) IX_INS(2) IX_INS(3) IX_INS(4) IX_INS(5) IX_INS(6) IX_INS(7) IX_INS(8) IX_INS(9) IX_INS(10) IX_INS(11) IX_INS(12) IX_INS(13) IX_INS(14) IX_INS(15)
;                                      IX_INS(16) IX_INS(17) IX_INS(18) IX_INS(19) IX_INS(20) IX_INS(21) IX_INS(22) IX_INS(23) IX_INS(24) IX_INS(25) IX_INS(26) IX_INS(27) IX_INS(28) IX_INS(29) IX_INS(30) IX_INS(31) default: break; }
.LBB0_1538:
	s_cmp_gt_u32 s58, 31
	s_cbranch_scc1 .LBB0_1630
	s_cmp_lt_i32 s58, 16
	s_cbranch_scc1 .Lib_0_8
	s_cmp_lt_i32 s58, 24
	s_cbranch_scc1 .Lib_8_12
	s_cmp_lt_i32 s58, 28
	s_cbranch_scc1 .Lib_12_14
	s_cmp_lt_i32 s58, 30
	s_cbranch_scc1 .Lib_14_15
	v_mov_b32_e32 v94, v238
	v_mov_b32_e32 v95, v239
	v_mov_b32_e32 v88, v0
	v_mov_b32_e32 v89, v1
	s_branch .LBB0_1630
.Lib_14_15:
	v_mov_b32_e32 v90, v238
	v_mov_b32_e32 v91, v239
	v_mov_b32_e32 v86, v0
	v_mov_b32_e32 v87, v1
	s_branch .LBB0_1630
.Lib_12_14:
	s_cmp_lt_i32 s58, 26
	s_cbranch_scc1 .Lib_12_13
	v_mov_b32_e32 v104, v238
	v_mov_b32_e32 v105, v239
	v_mov_b32_e32 v102, v0
	v_mov_b32_e32 v103, v1
	s_branch .LBB0_1630
.Lib_12_13:
	v_mov_b32_e32 v112, v238
	v_mov_b32_e32 v113, v239
	v_mov_b32_e32 v110, v0
	v_mov_b32_e32 v111, v1
	s_branch .LBB0_1630
.Lib_8_12:
	s_cmp_lt_i32 s58, 20
	s_cbranch_scc1 .Lib_8_10
	s_cmp_lt_i32 s58, 22
	s_cbranch_scc1 .Lib_10_11
	v_mov_b32_e32 v120, v238
	v_mov_b32_e32 v121, v239
	v_mov_b32_e32 v118, v0
	v_mov_b32_e32 v119, v1
	s_branch .LBB0_1630
.Lib_10_11:
	v_mov_b32_e32 v128, v238
	v_mov_b32_e32 v129, v239
	v_mov_b32_e32 v126, v0
	v_mov_b32_e32 v127, v1
	s_branch .LBB0_1630
.Lib_8_10:
	s_cmp_lt_i32 s58, 18
	s_cbranch_scc1 .Lib_8_9
	v_mov_b32_e32 v136, v238
	v_mov_b32_e32 v137, v239
	v_mov_b32_e32 v134, v0
	v_mov_b32_e32 v135, v1
	s_branch .LBB0_1630
.Lib_8_9:
	v_mov_b32_e32 v144, v238
	v_mov_b32_e32 v145, v239
	v_mov_b32_e32 v142, v0
	v_mov_b32_e32 v143, v1
	s_branch .LBB0_1630
.Lib_0_8:
	s_cmp_lt_i32 s58, 8
	s_cbranch_scc1 .Lib_0_4
	s_cmp_lt_i32 s58, 12
	s_cbranch_scc1 .Lib_4_6
	s_cmp_lt_i32 s58, 14
	s_cbranch_scc1 .Lib_6_7
	v_mov_b32_e32 v152, v238
	v_mov_b32_e32 v153, v239
	v_mov_b32_e32 v150, v0
	v_mov_b32_e32 v151, v1
	s_branch .LBB0_1630
.Lib_6_7:
	v_mov_b32_e32 v160, v238
	v_mov_b32_e32 v161, v239
	v_mov_b32_e32 v158, v0
	v_mov_b32_e32 v159, v1
	s_branch .LBB0_1630
.Lib_4_6:
	s_cmp_lt_i32 s58, 10
	s_cbranch_scc1 .Lib_4_5
	v_mov_b32_e32 v168, v238
	v_mov_b32_e32 v169, v239
	v_mov_b32_e32 v166, v0
	v_mov_b32_e32 v167, v1
	s_branch .LBB0_1630
.Lib_4_5:
	v_mov_b32_e32 v176, v238
	v_mov_b32_e32 v177, v239
	v_mov_b32_e32 v174, v0
	v_mov_b32_e32 v175, v1
	s_branch .LBB0_1630
.Lib_0_4:
	s_cmp_lt_i32 s58, 4
	s_cbranch_scc1 .Lib_0_2
	s_cmp_lt_i32 s58, 6
	s_cbranch_scc1 .Lib_2_3
	v_mov_b32_e32 v184, v238
	v_mov_b32_e32 v185, v239
	v_mov_b32_e32 v182, v0
	v_mov_b32_e32 v183, v1
	s_branch .LBB0_1630
.Lib_2_3:
	v_mov_b32_e32 v192, v238
	v_mov_b32_e32 v193, v239
	v_mov_b32_e32 v190, v0
	v_mov_b32_e32 v191, v1
	s_branch .LBB0_1630
.Lib_0_2:
	s_cmp_lt_i32 s58, 2
	s_cbranch_scc1 .Lib_0_1
	v_mov_b32_e32 v200, v238
	v_mov_b32_e32 v201, v239
	v_mov_b32_e32 v198, v0
	v_mov_b32_e32 v199, v1
	s_branch .LBB0_1630
.Lib_0_1:
	v_mov_b32_e32 v208, v238
	v_mov_b32_e32 v209, v239
	v_mov_b32_e32 v206, v0
	v_mov_b32_e32 v207, v1
